# speedup vs baseline: 1.0013x; 1.0013x over previous
.LBB3_3:
	s_add_u32 s42, s46, 0x3000
	s_addc_u32 s43, s47, 0
	s_add_u32 s44, s48, 0x0
	s_addc_u32 s45, s49, 0
	v_mov_b64_e32 v[30:31], v[14:15]
	v_mov_b64_e32 v[28:29], v[12:13]
	v_mov_b64_e32 v[26:27], v[10:11]
	v_mov_b64_e32 v[24:25], v[8:9]
	v_mov_b64_e32 v[22:23], v[6:7]
	v_mov_b64_e32 v[20:21], v[4:5]
	v_mov_b64_e32 v[18:19], v[2:3]
	v_mov_b64_e32 v[16:17], v[0:1]
	v_add_u32_e32 v32, s38, v201
	s_waitcnt vmcnt(0) lgkmcnt(0)
	s_barrier
	v_add_u32_e32 v41, v32, v200
	v_add_u32_e32 v40, v32, v195
	ds_read_b128 v[36:39], v41
	ds_read_b128 v[32:35], v40
	ds_read_b128 v[48:51], v40 offset:2048
	ds_read_b128 v[52:55], v41 offset:2048
	s_waitcnt vmcnt(0) lgkmcnt(0)
	v_mfma_scale_f32_32x32x64_f8f6f4 v[32:47], v[32:39], v[152:159], v[16:31], v173, v194 op_sel_hi:[0,0,0]
	s_waitcnt vmcnt(2) lgkmcnt(0)
	s_barrier
	s_xor_b64 s[28:29], s[30:31], -1
	s_mov_b32 s6, -1
	s_nop 15
	v_max_f32_e32 v56, v33, v33
	v_mfma_scale_f32_32x32x64_f8f6f4 v[16:31], v[48:55], v[152:159], v[16:31], v173, v194 op_sel_hi:[0,0,0]
	v_max_f32_e32 v57, v32, v32
	v_max_f32_e32 v56, v57, v56
	s_nop 15
	s_nop 1
	v_max3_f32 v48, v34, v35, v17
	v_max3_f32 v49, v56, v16, v18
	v_max3_f32 v49, v49, v19, v36
	v_max3_f32 v48, v48, v38, v39
	v_max3_f32 v48, v48, v22, v23
	v_max3_f32 v49, v49, v37, v20
	v_max3_f32 v48, v48, v42, v43
	v_max3_f32 v49, v49, v21, v40
	v_max3_f32 v48, v48, v26, v27
	v_max3_f32 v49, v49, v41, v24
	v_max3_f32 v48, v48, v46, v47
	v_max3_f32 v49, v49, v25, v44
	v_max3_f32 v48, v48, v30, v31
	v_max3_f32 v49, v49, v45, v28
	v_max3_f32 v48, v49, v29, v48
	v_mov_b32_e32 v49, v48
	s_nop 1
	v_permlane32_swap_b32_e32 v48, v49
	v_max_f32_e32 v49, v49, v49
	v_max_f32_e32 v48, v48, v48
	v_max_f32_e32 v48, v48, v49
	v_sub_f32_e32 v95, v47, v48
	v_sub_f32_e32 v94, v46, v48
	v_sub_f32_e32 v93, v45, v48
	v_sub_f32_e32 v92, v44, v48
	v_sub_f32_e32 v91, v43, v48
	v_sub_f32_e32 v90, v42, v48
	v_sub_f32_e32 v89, v41, v48
	v_sub_f32_e32 v88, v40, v48
	v_sub_f32_e32 v87, v39, v48
	v_sub_f32_e32 v86, v38, v48
	v_sub_f32_e32 v85, v37, v48
	v_sub_f32_e32 v84, v36, v48
	v_sub_f32_e32 v83, v35, v48
	v_sub_f32_e32 v82, v34, v48
	v_sub_f32_e32 v81, v33, v48
	v_sub_f32_e32 v80, v32, v48
	v_sub_f32_e32 v111, v31, v48
	v_sub_f32_e32 v110, v30, v48
	v_sub_f32_e32 v109, v29, v48
	v_sub_f32_e32 v108, v28, v48
	v_sub_f32_e32 v107, v27, v48
	v_sub_f32_e32 v106, v26, v48
	v_sub_f32_e32 v105, v25, v48
	v_sub_f32_e32 v104, v24, v48
	v_sub_f32_e32 v103, v23, v48
	v_sub_f32_e32 v102, v22, v48
	v_sub_f32_e32 v101, v21, v48
	v_sub_f32_e32 v100, v20, v48
	v_sub_f32_e32 v99, v19, v48
	v_sub_f32_e32 v98, v18, v48
	v_sub_f32_e32 v97, v17, v48
	v_sub_f32_e32 v96, v16, v48
	v_xor_b32_e32 v64, 0x80000000, v48
	v_mov_b64_e32 v[46:47], v[14:15]
	v_mov_b64_e32 v[30:31], v[14:15]
	v_mov_b64_e32 v[62:63], v[14:15]
	v_mov_b32_e32 v65, v64
	v_mov_b32_e32 v66, v64
	v_mov_b32_e32 v67, v64
	v_mov_b32_e32 v68, v64
	v_mov_b32_e32 v69, v64
	v_mov_b32_e32 v70, v64
	v_mov_b32_e32 v71, v64
	v_mov_b32_e32 v72, v64
	v_mov_b32_e32 v73, v64
	v_mov_b32_e32 v74, v64
	v_mov_b32_e32 v75, v64
	v_mov_b32_e32 v76, v64
	v_mov_b32_e32 v77, v64
	v_mov_b32_e32 v78, v64
	v_mov_b32_e32 v79, v64
	v_mov_b64_e32 v[44:45], v[12:13]
	v_mov_b64_e32 v[42:43], v[10:11]
	v_mov_b64_e32 v[40:41], v[8:9]
	v_mov_b64_e32 v[38:39], v[6:7]
	v_mov_b64_e32 v[36:37], v[4:5]
	v_mov_b64_e32 v[34:35], v[2:3]
	v_mov_b64_e32 v[32:33], v[0:1]
	v_mov_b64_e32 v[28:29], v[12:13]
	v_mov_b64_e32 v[26:27], v[10:11]
	v_mov_b64_e32 v[24:25], v[8:9]
	v_mov_b64_e32 v[22:23], v[6:7]
	v_mov_b64_e32 v[20:21], v[4:5]
	v_mov_b64_e32 v[18:19], v[2:3]
	v_mov_b64_e32 v[16:17], v[0:1]
	v_mov_b64_e32 v[60:61], v[12:13]
	v_mov_b64_e32 v[58:59], v[10:11]
	v_mov_b64_e32 v[56:57], v[8:9]
	v_mov_b64_e32 v[54:55], v[6:7]
	v_mov_b64_e32 v[52:53], v[4:5]
	v_mov_b64_e32 v[50:51], v[2:3]
	v_mov_b64_e32 v[48:49], v[0:1]
	s_mov_b32 s39, 0
	s_nop 0
